# v28
# baseline (speedup 1.0000x reference)
_Z7k_layerILb1EEvPKvPKhPKfPKiS7_PKDF16_S5_PvPhPf:
	s_load_dwordx8 s[8:15], s[0:1], 0x0
	s_load_dwordx4 s[4:7], s[0:1], 0x20
	s_load_dwordx2 s[16:17], s[0:1], 0x30
	v_and_b32_e32 v68, 63, v0
	v_lshrrev_b32_e32 v72, 6, v0
	v_bfe_u32 v1, v0, 4, 2
	v_and_b32_e32 v73, 15, v0
	s_setprio 0
	s_mul_i32 s18, s2, 60
	v_and_b32_e32 v75, 31, v0
	v_mad_u32_u24 v78, v72, 15, s18
	v_min_u32_e32 v2, 15, v75
	v_add_u32_e32 v2, v78, v2
	v_min_i32_e32 v2, 0x186a0, v2
	v_ashrrev_i32_e32 v3, 31, v2
	s_waitcnt lgkmcnt(0)
	v_lshl_add_u64 v[2:3], v[2:3], 2, s[14:15]
	global_load_dword v22, v[2:3], off
	v_lshl_or_b32 v74, v72, 5, v75
	v_lshlrev_b32_e32 v2, 2, v74
	global_load_dword v67, v2, s[16:17]
	v_and_b32_e32 v2, 0xc0, v0
	v_mov_b32_e32 v9, 0
	v_lshlrev_b32_e32 v8, 4, v2
	v_lshl_add_u64 v[10:11], s[6:7], 0, v[8:9]
	v_mul_u32_u24_e32 v77, 15, v72
	s_mov_b32 s16, 0x186a0
	s_mov_b32 s17, 0
	s_mov_b64 s[2:3], -1
	v_mbcnt_lo_u32_b32 v23, -1, 0
	v_add_u32_e32 v76, v1, v77
	v_lshlrev_b32_e32 v8, 4, v68
	v_lshlrev_b32_e32 v66, 3, v73
	v_lshlrev_b32_e32 v6, 5, v73
	s_waitcnt vmcnt(1)
	v_readlane_b32 s6, v22, 0
	v_readlane_b32 s7, v22, 16
	s_sub_i32 s19, s7, s6
	s_cmpk_lt_i32 s19, 0x181
	s_cbranch_scc1 .LBB2_12
	v_mbcnt_hi_u32_b32 v2, -1, v23
	v_and_b32_e32 v24, 64, v2
	v_mov_b32_e32 v7, v9
	v_or_b32_e32 v25, 1, v24
	v_lshl_add_u64 v[12:13], s[8:9], 0, v[6:7]
	s_mov_b32 s7, 0x64646464
	v_mov_b32_e32 v7, 0x4010400
	v_mov_b32_e32 v26, 0x4030402
	s_branch .LBB2_4

_Z7k_layerILb0EEvPKvPKhPKfPKiS7_PKDF16_S5_PvPhPf:
	s_load_dwordx8 s[8:15], s[0:1], 0x0
	s_load_dwordx4 s[4:7], s[0:1], 0x20
	s_load_dwordx2 s[18:19], s[0:1], 0x30
	v_and_b32_e32 v66, 63, v0
	v_lshrrev_b32_e32 v18, 6, v0
	v_bfe_u32 v73, v0, 4, 2
	v_and_b32_e32 v71, 15, v0
	s_setprio 0
	s_mul_i32 s16, s2, 60
	v_and_b32_e32 v72, 31, v0
	v_mad_u32_u24 v76, v18, 15, s16
	v_min_u32_e32 v1, 15, v72
	v_add_u32_e32 v1, v76, v1
	v_min_i32_e32 v2, 0x186a0, v1
	v_ashrrev_i32_e32 v3, 31, v2
	s_waitcnt lgkmcnt(0)
	v_lshl_add_u64 v[2:3], v[2:3], 2, s[14:15]
	global_load_dword v22, v[2:3], off
	v_lshl_or_b32 v1, v18, 5, v72
	v_lshlrev_b32_e32 v1, 2, v1
	global_load_dword v70, v1, s[18:19]
	v_and_b32_e32 v2, 0xc0, v0
	v_mov_b32_e32 v3, 0
	v_lshlrev_b32_e32 v2, 4, v2
	v_lshl_add_u64 v[4:5], s[6:7], 0, v[2:3]
	v_mul_u32_u24_e32 v75, 15, v18
	s_mov_b32 s18, 0
	s_mov_b64 s[2:3], -1
	v_mbcnt_lo_u32_b32 v19, -1, 0
	v_add_u32_e32 v74, v73, v75
	v_lshlrev_b32_e32 v2, 4, v66
	v_lshlrev_b32_e32 v78, 3, v71
	v_lshlrev_b32_e32 v77, 4, v71
	s_waitcnt vmcnt(1)
	v_readlane_b32 s6, v22, 0
	v_readlane_b32 s7, v22, 16
	s_sub_i32 s17, s7, s6
	s_cmpk_lt_i32 s17, 0x181
	s_cbranch_scc1 .LBB3_10
	v_mbcnt_hi_u32_b32 v6, -1, v19
	v_and_b32_e32 v20, 64, v6
	v_or_b32_e32 v21, 1, v20
	s_mov_b32 s7, 0x64646464
	v_mov_b32_e32 v23, 0x4010400
	v_mov_b32_e32 v24, 0x4030402
	s_branch .LBB3_3
